# speedup vs baseline: 1.0481x; 1.0481x over previous
.Lpc_anchor:
	s_add_u32 s44, s44, _Z7dog_finPKfS0_Pf-.Lpc_anchor
	s_addc_u32 s45, s45, 0
	s_load_dwordx16 s[48:63], s[44:45], 0x0
	s_load_dwordx16 s[64:79], s[44:45], 0x40
	s_load_dwordx16 s[80:95], s[44:45], 0x80
	s_and_b32 s46, s0, 0xfff
	s_cmp_lt_u32 s46, 0xec0
	s_cbranch_scc0 .Lno_karg_touch
	s_load_dwordx16 s[48:63], s[0:1], 0x40
	s_load_dwordx16 s[64:79], s[0:1], 0x80
	s_load_dwordx16 s[80:95], s[0:1], 0xc0
	s_load_dwordx16 s[48:63], s[0:1], 0x100
.Lno_karg_touch:
	v_mul_f32_e32 v16, v12, v12
	v_add_f32_e32 v17, 0x3f800000, v12
	v_add_f32_e32 v18, 0x40000000, v12
	v_add_f32_e32 v19, 0x40400000, v12
	v_mul_f32_e32 v17, v17, v17
	v_mul_f32_e32 v18, v18, v18
	v_mul_f32_e32 v19, v19, v19
	v_mul_f32_e32 v20, v8, v16
	v_mul_f32_e32 v24, v9, v16
	v_mul_f32_e32 v21, v8, v17
	v_mul_f32_e32 v25, v9, v17
	v_mul_f32_e32 v22, v8, v18
	v_mul_f32_e32 v26, v9, v18
	v_mul_f32_e32 v23, v8, v19
	v_mul_f32_e32 v27, v9, v19
	v_exp_f32_e32 v20, v20
	v_exp_f32_e32 v21, v21
	v_exp_f32_e32 v22, v22
	v_exp_f32_e32 v23, v23
	v_exp_f32_e32 v24, v24
	v_exp_f32_e32 v25, v25
	v_exp_f32_e32 v26, v26
	v_exp_f32_e32 v27, v27
	v_cvt_pk_f16_f32 v32, v20, v21
	v_cvt_pk_f16_f32 v33, v22, v23
	v_cvt_pk_f16_f32 v64, v24, v25
	v_cvt_pk_f16_f32 v65, v26, v27
	v_add_f32_e32 v16, 0x40800000, v12
	v_add_f32_e32 v17, 0x40a00000, v12
	v_add_f32_e32 v18, 0x40c00000, v12
	v_add_f32_e32 v19, 0x40e00000, v12
	v_mul_f32_e32 v16, v16, v16
	v_mul_f32_e32 v17, v17, v17
	v_mul_f32_e32 v18, v18, v18
	v_mul_f32_e32 v19, v19, v19
	v_mul_f32_e32 v20, v8, v16
	v_mul_f32_e32 v24, v9, v16
	v_mul_f32_e32 v21, v8, v17
	v_mul_f32_e32 v25, v9, v17
	v_mul_f32_e32 v22, v8, v18
	v_mul_f32_e32 v26, v9, v18
	v_mul_f32_e32 v23, v8, v19
	v_mul_f32_e32 v27, v9, v19
	v_exp_f32_e32 v20, v20
	v_exp_f32_e32 v21, v21
	v_exp_f32_e32 v22, v22
	v_exp_f32_e32 v23, v23
	v_exp_f32_e32 v24, v24
	v_exp_f32_e32 v25, v25
	v_exp_f32_e32 v26, v26
	v_exp_f32_e32 v27, v27
	v_cvt_pk_f16_f32 v34, v20, v21
	v_cvt_pk_f16_f32 v35, v22, v23
	v_cvt_pk_f16_f32 v66, v24, v25
	v_cvt_pk_f16_f32 v67, v26, v27
	v_add_f32_e32 v16, 0x42000000, v12
	v_add_f32_e32 v17, 0x42040000, v12
	v_add_f32_e32 v18, 0x42080000, v12
	v_add_f32_e32 v19, 0x420c0000, v12
	v_mul_f32_e32 v16, v16, v16
	v_mul_f32_e32 v17, v17, v17
	v_mul_f32_e32 v18, v18, v18
	v_mul_f32_e32 v19, v19, v19
	v_mul_f32_e32 v20, v8, v16
	v_mul_f32_e32 v24, v9, v16
	v_mul_f32_e32 v21, v8, v17
	v_mul_f32_e32 v25, v9, v17
	v_mul_f32_e32 v22, v8, v18
	v_mul_f32_e32 v26, v9, v18
	v_mul_f32_e32 v23, v8, v19
	v_mul_f32_e32 v27, v9, v19
	v_exp_f32_e32 v20, v20
	v_exp_f32_e32 v21, v21
	v_exp_f32_e32 v22, v22
	v_exp_f32_e32 v23, v23
	v_exp_f32_e32 v24, v24
	v_exp_f32_e32 v25, v25
	v_exp_f32_e32 v26, v26
	v_exp_f32_e32 v27, v27
	v_cvt_pk_f16_f32 v36, v20, v21
	v_cvt_pk_f16_f32 v37, v22, v23
	v_cvt_pk_f16_f32 v68, v24, v25
	v_cvt_pk_f16_f32 v69, v26, v27
	v_add_f32_e32 v16, 0x42100000, v12
	v_add_f32_e32 v17, 0x42140000, v12
	v_add_f32_e32 v18, 0x42180000, v12
	v_add_f32_e32 v19, 0x421c0000, v12
	v_mul_f32_e32 v16, v16, v16
	v_mul_f32_e32 v17, v17, v17
	v_mul_f32_e32 v18, v18, v18
	v_mul_f32_e32 v19, v19, v19
	v_mul_f32_e32 v20, v8, v16
	v_mul_f32_e32 v24, v9, v16
	v_mul_f32_e32 v21, v8, v17
	v_mul_f32_e32 v25, v9, v17
	v_mul_f32_e32 v22, v8, v18
	v_mul_f32_e32 v26, v9, v18
	v_mul_f32_e32 v23, v8, v19
	v_mul_f32_e32 v27, v9, v19
	v_exp_f32_e32 v20, v20
	v_exp_f32_e32 v21, v21
	v_exp_f32_e32 v22, v22
	v_exp_f32_e32 v23, v23
	v_exp_f32_e32 v24, v24
	v_exp_f32_e32 v25, v25
	v_exp_f32_e32 v26, v26
	v_exp_f32_e32 v27, v27
	v_cvt_pk_f16_f32 v38, v20, v21
	v_cvt_pk_f16_f32 v39, v22, v23
	v_cvt_pk_f16_f32 v70, v24, v25
	v_cvt_pk_f16_f32 v71, v26, v27
	v_add_u32_e32 v6, 0x8000, v6
	global_load_dwordx4 v[160:163], v6, s[12:13] offset:0 nt
	global_load_dwordx4 v[164:167], v6, s[12:13] offset:1024 nt
	global_load_dwordx4 v[168:171], v6, s[12:13] offset:2048 nt
	global_load_dwordx4 v[172:175], v6, s[12:13] offset:3072 nt
	v_add_f32_e32 v16, 0x42800000, v12
	v_add_f32_e32 v17, 0x42820000, v12
	v_add_f32_e32 v18, 0x42840000, v12
	v_add_f32_e32 v19, 0x42860000, v12
	v_mul_f32_e32 v16, v16, v16
	v_mul_f32_e32 v17, v17, v17
	v_mul_f32_e32 v18, v18, v18
	v_mul_f32_e32 v19, v19, v19
	v_mul_f32_e32 v20, v8, v16
	v_mul_f32_e32 v24, v9, v16
	v_mul_f32_e32 v21, v8, v17
	v_mul_f32_e32 v25, v9, v17
	v_mul_f32_e32 v22, v8, v18
	v_mul_f32_e32 v26, v9, v18
	v_mul_f32_e32 v23, v8, v19
	v_mul_f32_e32 v27, v9, v19
	v_exp_f32_e32 v20, v20
	v_exp_f32_e32 v21, v21
	v_exp_f32_e32 v22, v22
	v_exp_f32_e32 v23, v23
	v_exp_f32_e32 v24, v24
	v_exp_f32_e32 v25, v25
	v_exp_f32_e32 v26, v26
	v_exp_f32_e32 v27, v27
	v_cvt_pk_f16_f32 v40, v20, v21
	v_cvt_pk_f16_f32 v41, v22, v23
	v_cvt_pk_f16_f32 v72, v24, v25
	v_cvt_pk_f16_f32 v73, v26, v27
	v_add_f32_e32 v16, 0x42880000, v12
	v_add_f32_e32 v17, 0x428a0000, v12
	v_add_f32_e32 v18, 0x428c0000, v12
	v_add_f32_e32 v19, 0x428e0000, v12
	v_mul_f32_e32 v16, v16, v16
	v_mul_f32_e32 v17, v17, v17
	v_mul_f32_e32 v18, v18, v18
	v_mul_f32_e32 v19, v19, v19
	v_mul_f32_e32 v20, v8, v16
	v_mul_f32_e32 v24, v9, v16
	v_mul_f32_e32 v21, v8, v17
	v_mul_f32_e32 v25, v9, v17
	v_mul_f32_e32 v22, v8, v18
	v_mul_f32_e32 v26, v9, v18
	v_mul_f32_e32 v23, v8, v19
	v_mul_f32_e32 v27, v9, v19
	v_exp_f32_e32 v20, v20
	v_exp_f32_e32 v21, v21
	v_exp_f32_e32 v22, v22
	v_exp_f32_e32 v23, v23
	v_exp_f32_e32 v24, v24
	v_exp_f32_e32 v25, v25
	v_exp_f32_e32 v26, v26
	v_exp_f32_e32 v27, v27
	v_cvt_pk_f16_f32 v42, v20, v21
	v_cvt_pk_f16_f32 v43, v22, v23
	v_cvt_pk_f16_f32 v74, v24, v25
	v_cvt_pk_f16_f32 v75, v26, v27
	v_add_f32_e32 v16, 0x42c00000, v12
	v_add_f32_e32 v17, 0x42c20000, v12
	v_add_f32_e32 v18, 0x42c40000, v12
	v_add_f32_e32 v19, 0x42c60000, v12
	v_mul_f32_e32 v16, v16, v16
	v_mul_f32_e32 v17, v17, v17
	v_mul_f32_e32 v18, v18, v18
	v_mul_f32_e32 v19, v19, v19
	v_mul_f32_e32 v20, v8, v16
	v_mul_f32_e32 v24, v9, v16
	v_mul_f32_e32 v21, v8, v17
	v_mul_f32_e32 v25, v9, v17
	v_mul_f32_e32 v22, v8, v18
	v_mul_f32_e32 v26, v9, v18
	v_mul_f32_e32 v23, v8, v19
	v_mul_f32_e32 v27, v9, v19
	v_exp_f32_e32 v20, v20
	v_exp_f32_e32 v21, v21
	v_exp_f32_e32 v22, v22
	v_exp_f32_e32 v23, v23
	v_exp_f32_e32 v24, v24
	v_exp_f32_e32 v25, v25
	v_exp_f32_e32 v26, v26
	v_exp_f32_e32 v27, v27
	v_cvt_pk_f16_f32 v44, v20, v21
	v_cvt_pk_f16_f32 v45, v22, v23
	v_cvt_pk_f16_f32 v76, v24, v25
	v_cvt_pk_f16_f32 v77, v26, v27
	v_add_f32_e32 v16, 0x42c80000, v12
	v_add_f32_e32 v17, 0x42ca0000, v12
	v_add_f32_e32 v18, 0x42cc0000, v12
	v_add_f32_e32 v19, 0x42ce0000, v12
	v_mul_f32_e32 v16, v16, v16
	v_mul_f32_e32 v17, v17, v17
	v_mul_f32_e32 v18, v18, v18
	v_mul_f32_e32 v19, v19, v19
	v_mul_f32_e32 v20, v8, v16
	v_mul_f32_e32 v24, v9, v16
	v_mul_f32_e32 v21, v8, v17
	v_mul_f32_e32 v25, v9, v17
	v_mul_f32_e32 v22, v8, v18
	v_mul_f32_e32 v26, v9, v18
	v_mul_f32_e32 v23, v8, v19
	v_mul_f32_e32 v27, v9, v19
	v_exp_f32_e32 v20, v20
	v_exp_f32_e32 v21, v21
	v_exp_f32_e32 v22, v22
	v_exp_f32_e32 v23, v23
	v_exp_f32_e32 v24, v24
	v_exp_f32_e32 v25, v25
	v_exp_f32_e32 v26, v26
	v_exp_f32_e32 v27, v27
	v_cvt_pk_f16_f32 v46, v20, v21
	v_cvt_pk_f16_f32 v47, v22, v23
	v_cvt_pk_f16_f32 v78, v24, v25
	v_cvt_pk_f16_f32 v79, v26, v27
	v_add_u32_e32 v6, 0x8000, v6
	global_load_dwordx4 v[176:179], v6, s[12:13] offset:0 nt
	global_load_dwordx4 v[180:183], v6, s[12:13] offset:1024 nt
	global_load_dwordx4 v[184:187], v6, s[12:13] offset:2048 nt
	global_load_dwordx4 v[188:191], v6, s[12:13] offset:3072 nt
	v_mul_f32_e32 v16, v2, v2
	v_add_f32_e32 v17, 0x3f800000, v2
	v_add_f32_e32 v18, 0x40000000, v2
	v_add_f32_e32 v19, 0x40400000, v2
	v_mul_f32_e32 v17, v17, v17
	v_mul_f32_e32 v18, v18, v18
	v_mul_f32_e32 v19, v19, v19
	v_mul_f32_e32 v20, v28, v16
	v_mul_f32_e32 v24, v29, v16
	v_mul_f32_e32 v21, v28, v17
	v_mul_f32_e32 v25, v29, v17
	v_mul_f32_e32 v22, v28, v18
	v_mul_f32_e32 v26, v29, v18
	v_mul_f32_e32 v23, v28, v19
	v_mul_f32_e32 v27, v29, v19
	v_exp_f32_e32 v20, v20
	v_exp_f32_e32 v21, v21
	v_exp_f32_e32 v22, v22
	v_exp_f32_e32 v23, v23
	v_exp_f32_e32 v24, v24
	v_exp_f32_e32 v25, v25
	v_exp_f32_e32 v26, v26
	v_exp_f32_e32 v27, v27
	v_cvt_pk_f16_f32 v48, v20, v21
	v_cvt_pk_f16_f32 v49, v22, v23
	v_cvt_pk_f16_f32 v80, v24, v25
	v_cvt_pk_f16_f32 v81, v26, v27
	v_add_f32_e32 v16, 0x40800000, v2
	v_add_f32_e32 v17, 0x40a00000, v2
	v_add_f32_e32 v18, 0x40c00000, v2
	v_add_f32_e32 v19, 0x40e00000, v2
	v_mul_f32_e32 v16, v16, v16
	v_mul_f32_e32 v17, v17, v17
	v_mul_f32_e32 v18, v18, v18
	v_mul_f32_e32 v19, v19, v19
	v_mul_f32_e32 v20, v28, v16
	v_mul_f32_e32 v24, v29, v16
	v_mul_f32_e32 v21, v28, v17
	v_mul_f32_e32 v25, v29, v17
	v_mul_f32_e32 v22, v28, v18
	v_mul_f32_e32 v26, v29, v18
	v_mul_f32_e32 v23, v28, v19
	v_mul_f32_e32 v27, v29, v19
	v_exp_f32_e32 v20, v20
	v_exp_f32_e32 v21, v21
	v_exp_f32_e32 v22, v22
	v_exp_f32_e32 v23, v23
	v_exp_f32_e32 v24, v24
	v_exp_f32_e32 v25, v25
	v_exp_f32_e32 v26, v26
	v_exp_f32_e32 v27, v27
	v_cvt_pk_f16_f32 v50, v20, v21
	v_cvt_pk_f16_f32 v51, v22, v23
	v_cvt_pk_f16_f32 v82, v24, v25
	v_cvt_pk_f16_f32 v83, v26, v27
	v_add_f32_e32 v16, 0x42000000, v2
	v_add_f32_e32 v17, 0x42040000, v2
	v_add_f32_e32 v18, 0x42080000, v2
	v_add_f32_e32 v19, 0x420c0000, v2
	v_mul_f32_e32 v16, v16, v16
	v_mul_f32_e32 v17, v17, v17
	v_mul_f32_e32 v18, v18, v18
	v_mul_f32_e32 v19, v19, v19
	v_mul_f32_e32 v20, v28, v16
	v_mul_f32_e32 v24, v29, v16
	v_mul_f32_e32 v21, v28, v17
	v_mul_f32_e32 v25, v29, v17
	v_mul_f32_e32 v22, v28, v18
	v_mul_f32_e32 v26, v29, v18
	v_mul_f32_e32 v23, v28, v19
	v_mul_f32_e32 v27, v29, v19
	v_exp_f32_e32 v20, v20
	v_exp_f32_e32 v21, v21
	v_exp_f32_e32 v22, v22
	v_exp_f32_e32 v23, v23
	v_exp_f32_e32 v24, v24
	v_exp_f32_e32 v25, v25
	v_exp_f32_e32 v26, v26
	v_exp_f32_e32 v27, v27
	v_cvt_pk_f16_f32 v52, v20, v21
	v_cvt_pk_f16_f32 v53, v22, v23
	v_cvt_pk_f16_f32 v84, v24, v25
	v_cvt_pk_f16_f32 v85, v26, v27
	v_add_f32_e32 v16, 0x42100000, v2
	v_add_f32_e32 v17, 0x42140000, v2
	v_add_f32_e32 v18, 0x42180000, v2
	v_add_f32_e32 v19, 0x421c0000, v2
	v_mul_f32_e32 v16, v16, v16
	v_mul_f32_e32 v17, v17, v17
	v_mul_f32_e32 v18, v18, v18
	v_mul_f32_e32 v19, v19, v19
	v_mul_f32_e32 v20, v28, v16
	v_mul_f32_e32 v24, v29, v16
	v_mul_f32_e32 v21, v28, v17
	v_mul_f32_e32 v25, v29, v17
	v_mul_f32_e32 v22, v28, v18
	v_mul_f32_e32 v26, v29, v18
	v_mul_f32_e32 v23, v28, v19
	v_mul_f32_e32 v27, v29, v19
	v_exp_f32_e32 v20, v20
	v_exp_f32_e32 v21, v21
	v_exp_f32_e32 v22, v22
	v_exp_f32_e32 v23, v23
	v_exp_f32_e32 v24, v24
	v_exp_f32_e32 v25, v25
	v_exp_f32_e32 v26, v26
	v_exp_f32_e32 v27, v27
	v_cvt_pk_f16_f32 v54, v20, v21
	v_cvt_pk_f16_f32 v55, v22, v23
	v_cvt_pk_f16_f32 v86, v24, v25
	v_cvt_pk_f16_f32 v87, v26, v27
	v_add_u32_e32 v6, 0x8000, v6
	global_load_dwordx4 v[192:195], v6, s[12:13] offset:0 nt
	global_load_dwordx4 v[196:199], v6, s[12:13] offset:1024 nt
	global_load_dwordx4 v[200:203], v6, s[12:13] offset:2048 nt
	global_load_dwordx4 v[204:207], v6, s[12:13] offset:3072 nt
	v_add_f32_e32 v16, 0x42800000, v2
	v_add_f32_e32 v17, 0x42820000, v2
	v_add_f32_e32 v18, 0x42840000, v2
	v_add_f32_e32 v19, 0x42860000, v2
	v_mul_f32_e32 v16, v16, v16
	v_mul_f32_e32 v17, v17, v17
	v_mul_f32_e32 v18, v18, v18
	v_mul_f32_e32 v19, v19, v19
	v_mul_f32_e32 v20, v28, v16
	v_mul_f32_e32 v24, v29, v16
	v_mul_f32_e32 v21, v28, v17
	v_mul_f32_e32 v25, v29, v17
	v_mul_f32_e32 v22, v28, v18
	v_mul_f32_e32 v26, v29, v18
	v_mul_f32_e32 v23, v28, v19
	v_mul_f32_e32 v27, v29, v19
	v_exp_f32_e32 v20, v20
	v_exp_f32_e32 v21, v21
	v_exp_f32_e32 v22, v22
	v_exp_f32_e32 v23, v23
	v_exp_f32_e32 v24, v24
	v_exp_f32_e32 v25, v25
	v_exp_f32_e32 v26, v26
	v_exp_f32_e32 v27, v27
	v_cvt_pk_f16_f32 v56, v20, v21
	v_cvt_pk_f16_f32 v57, v22, v23
	v_cvt_pk_f16_f32 v88, v24, v25
	v_cvt_pk_f16_f32 v89, v26, v27
	v_add_f32_e32 v16, 0x42880000, v2
	v_add_f32_e32 v17, 0x428a0000, v2
	v_add_f32_e32 v18, 0x428c0000, v2
	v_add_f32_e32 v19, 0x428e0000, v2
	v_mul_f32_e32 v16, v16, v16
	v_mul_f32_e32 v17, v17, v17
	v_mul_f32_e32 v18, v18, v18
	v_mul_f32_e32 v19, v19, v19
	v_mul_f32_e32 v20, v28, v16
	v_mul_f32_e32 v24, v29, v16
	v_mul_f32_e32 v21, v28, v17
	v_mul_f32_e32 v25, v29, v17
	v_mul_f32_e32 v22, v28, v18
	v_mul_f32_e32 v26, v29, v18
	v_mul_f32_e32 v23, v28, v19
	v_mul_f32_e32 v27, v29, v19
	v_exp_f32_e32 v20, v20
	v_exp_f32_e32 v21, v21
	v_exp_f32_e32 v22, v22
	v_exp_f32_e32 v23, v23
	v_exp_f32_e32 v24, v24
	v_exp_f32_e32 v25, v25
	v_exp_f32_e32 v26, v26
	v_exp_f32_e32 v27, v27
	v_cvt_pk_f16_f32 v58, v20, v21
	v_cvt_pk_f16_f32 v59, v22, v23
	v_cvt_pk_f16_f32 v90, v24, v25
	v_cvt_pk_f16_f32 v91, v26, v27
	v_add_f32_e32 v16, 0x42c00000, v2
	v_add_f32_e32 v17, 0x42c20000, v2
	v_add_f32_e32 v18, 0x42c40000, v2
	v_add_f32_e32 v19, 0x42c60000, v2
	v_mul_f32_e32 v16, v16, v16
	v_mul_f32_e32 v17, v17, v17
	v_mul_f32_e32 v18, v18, v18
	v_mul_f32_e32 v19, v19, v19
	v_mul_f32_e32 v20, v28, v16
	v_mul_f32_e32 v24, v29, v16
	v_mul_f32_e32 v21, v28, v17
	v_mul_f32_e32 v25, v29, v17
	v_mul_f32_e32 v22, v28, v18
	v_mul_f32_e32 v26, v29, v18
	v_mul_f32_e32 v23, v28, v19
	v_mul_f32_e32 v27, v29, v19
	v_exp_f32_e32 v20, v20
	v_exp_f32_e32 v21, v21
	v_exp_f32_e32 v22, v22
	v_exp_f32_e32 v23, v23
	v_exp_f32_e32 v24, v24
	v_exp_f32_e32 v25, v25
	v_exp_f32_e32 v26, v26
	v_exp_f32_e32 v27, v27
	v_cvt_pk_f16_f32 v60, v20, v21
	v_cvt_pk_f16_f32 v61, v22, v23
	v_cvt_pk_f16_f32 v92, v24, v25
	v_cvt_pk_f16_f32 v93, v26, v27
	v_add_f32_e32 v16, 0x42c80000, v2
	v_add_f32_e32 v17, 0x42ca0000, v2
	v_add_f32_e32 v18, 0x42cc0000, v2
	v_add_f32_e32 v19, 0x42ce0000, v2
	v_mul_f32_e32 v16, v16, v16
	v_mul_f32_e32 v17, v17, v17
	v_mul_f32_e32 v18, v18, v18
	v_mul_f32_e32 v19, v19, v19
	v_mul_f32_e32 v20, v28, v16
	v_mul_f32_e32 v24, v29, v16
	v_mul_f32_e32 v21, v28, v17
	v_mul_f32_e32 v25, v29, v17
	v_mul_f32_e32 v22, v28, v18
	v_mul_f32_e32 v26, v29, v18
	v_mul_f32_e32 v23, v28, v19
	v_mul_f32_e32 v27, v29, v19
	v_exp_f32_e32 v20, v20
	v_exp_f32_e32 v21, v21
	v_exp_f32_e32 v22, v22
	v_exp_f32_e32 v23, v23
	v_exp_f32_e32 v24, v24
	v_exp_f32_e32 v25, v25
	v_exp_f32_e32 v26, v26
	v_exp_f32_e32 v27, v27
	v_cvt_pk_f16_f32 v62, v20, v21
	v_cvt_pk_f16_f32 v63, v22, v23
	v_cvt_pk_f16_f32 v94, v24, v25
	v_cvt_pk_f16_f32 v95, v26, v27
	v_add_u32_e32 v6, 0x8000, v6
	global_load_dwordx4 v[208:211], v6, s[12:13] offset:0 nt
	global_load_dwordx4 v[212:215], v6, s[12:13] offset:1024 nt
	global_load_dwordx4 v[216:219], v6, s[12:13] offset:2048 nt
	global_load_dwordx4 v[220:223], v6, s[12:13] offset:3072 nt
	v_mul_f32_e32 v16, v13, v13
	v_add_f32_e32 v17, 0x3f800000, v13
	v_add_f32_e32 v18, 0x40000000, v13
	v_add_f32_e32 v19, 0x40400000, v13
	v_mul_f32_e32 v17, v17, v17
	v_mul_f32_e32 v18, v18, v18
	v_mul_f32_e32 v19, v19, v19
	v_mul_f32_e32 v20, v8, v16
	v_mul_f32_e32 v24, v9, v16
	v_mul_f32_e32 v21, v8, v17
	v_mul_f32_e32 v25, v9, v17
	v_mul_f32_e32 v22, v8, v18
	v_mul_f32_e32 v26, v9, v18
	v_mul_f32_e32 v23, v8, v19
	v_mul_f32_e32 v27, v9, v19
	v_exp_f32_e32 v20, v20
	v_exp_f32_e32 v21, v21
	v_exp_f32_e32 v22, v22
	v_exp_f32_e32 v23, v23
	v_exp_f32_e32 v24, v24
	v_exp_f32_e32 v25, v25
	v_exp_f32_e32 v26, v26
	v_exp_f32_e32 v27, v27
	v_mul_f32_e32 v96, v10, v20
	v_mul_f32_e32 v97, v10, v21
	v_mul_f32_e32 v98, v10, v22
	v_mul_f32_e32 v99, v10, v23
	v_mul_f32_e32 v112, v11, v24
	v_mul_f32_e32 v113, v11, v25
	v_mul_f32_e32 v114, v11, v26
	v_mul_f32_e32 v115, v11, v27
	v_add_f32_e32 v16, 0x41800000, v13
	v_add_f32_e32 v17, 0x41880000, v13
	v_add_f32_e32 v18, 0x41900000, v13
	v_add_f32_e32 v19, 0x41980000, v13
	v_mul_f32_e32 v16, v16, v16
	v_mul_f32_e32 v17, v17, v17
	v_mul_f32_e32 v18, v18, v18
	v_mul_f32_e32 v19, v19, v19
	v_mul_f32_e32 v20, v8, v16
	v_mul_f32_e32 v24, v9, v16
	v_mul_f32_e32 v21, v8, v17
	v_mul_f32_e32 v25, v9, v17
	v_mul_f32_e32 v22, v8, v18
	v_mul_f32_e32 v26, v9, v18
	v_mul_f32_e32 v23, v8, v19
	v_mul_f32_e32 v27, v9, v19
	v_exp_f32_e32 v20, v20
	v_exp_f32_e32 v21, v21
	v_exp_f32_e32 v22, v22
	v_exp_f32_e32 v23, v23
	v_exp_f32_e32 v24, v24
	v_exp_f32_e32 v25, v25
	v_exp_f32_e32 v26, v26
	v_exp_f32_e32 v27, v27
	v_mul_f32_e32 v100, v10, v20
	v_mul_f32_e32 v101, v10, v21
	v_mul_f32_e32 v102, v10, v22
	v_mul_f32_e32 v103, v10, v23
	v_mul_f32_e32 v116, v11, v24
	v_mul_f32_e32 v117, v11, v25
	v_mul_f32_e32 v118, v11, v26
	v_mul_f32_e32 v119, v11, v27
	v_add_u32_e32 v6, 0x8000, v6
	global_load_dwordx4 v[224:227], v6, s[12:13] offset:0 nt
	global_load_dwordx4 v[228:231], v6, s[12:13] offset:1024 nt
	global_load_dwordx4 v[232:235], v6, s[12:13] offset:2048 nt
	global_load_dwordx4 v[236:239], v6, s[12:13] offset:3072 nt
	v_mul_f32_e32 v16, v3, v3
	v_add_f32_e32 v17, 0x3f800000, v3
	v_add_f32_e32 v18, 0x40000000, v3
	v_add_f32_e32 v19, 0x40400000, v3
	v_mul_f32_e32 v17, v17, v17
	v_mul_f32_e32 v18, v18, v18
	v_mul_f32_e32 v19, v19, v19
	v_mul_f32_e32 v20, v28, v16
	v_mul_f32_e32 v24, v29, v16
	v_mul_f32_e32 v21, v28, v17
	v_mul_f32_e32 v25, v29, v17
	v_mul_f32_e32 v22, v28, v18
	v_mul_f32_e32 v26, v29, v18
	v_mul_f32_e32 v23, v28, v19
	v_mul_f32_e32 v27, v29, v19
	v_exp_f32_e32 v20, v20
	v_exp_f32_e32 v21, v21
	v_exp_f32_e32 v22, v22
	v_exp_f32_e32 v23, v23
	v_exp_f32_e32 v24, v24
	v_exp_f32_e32 v25, v25
	v_exp_f32_e32 v26, v26
	v_exp_f32_e32 v27, v27
	v_mul_f32_e32 v104, v30, v20
	v_mul_f32_e32 v105, v30, v21
	v_mul_f32_e32 v106, v30, v22
	v_mul_f32_e32 v107, v30, v23
	v_mul_f32_e32 v120, v31, v24
	v_mul_f32_e32 v121, v31, v25
	v_mul_f32_e32 v122, v31, v26
	v_mul_f32_e32 v123, v31, v27
	v_add_f32_e32 v16, 0x41800000, v3
	v_add_f32_e32 v17, 0x41880000, v3
	v_add_f32_e32 v18, 0x41900000, v3
	v_add_f32_e32 v19, 0x41980000, v3
	v_mul_f32_e32 v16, v16, v16
	v_mul_f32_e32 v17, v17, v17
	v_mul_f32_e32 v18, v18, v18
	v_mul_f32_e32 v19, v19, v19
	v_mul_f32_e32 v20, v28, v16
	v_mul_f32_e32 v24, v29, v16
	v_mul_f32_e32 v21, v28, v17
	v_mul_f32_e32 v25, v29, v17
	v_mul_f32_e32 v22, v28, v18
	v_mul_f32_e32 v26, v29, v18
	v_mul_f32_e32 v23, v28, v19
	v_mul_f32_e32 v27, v29, v19
	v_exp_f32_e32 v20, v20
	v_exp_f32_e32 v21, v21
	v_exp_f32_e32 v22, v22
	v_exp_f32_e32 v23, v23
	v_exp_f32_e32 v24, v24
	v_exp_f32_e32 v25, v25
	v_exp_f32_e32 v26, v26
	v_exp_f32_e32 v27, v27
	v_mul_f32_e32 v108, v30, v20
	v_mul_f32_e32 v109, v30, v21
	v_mul_f32_e32 v110, v30, v22
	v_mul_f32_e32 v111, v30, v23
	v_mul_f32_e32 v124, v31, v24
	v_mul_f32_e32 v125, v31, v25
	v_mul_f32_e32 v126, v31, v26
	v_mul_f32_e32 v127, v31, v27
	v_add_u32_e32 v6, 0x8000, v6
	global_load_dwordx4 v[240:243], v6, s[12:13] offset:0 nt
	global_load_dwordx4 v[244:247], v6, s[12:13] offset:1024 nt
	global_load_dwordx4 v[248:251], v6, s[12:13] offset:2048 nt
	global_load_dwordx4 v[252:255], v6, s[12:13] offset:3072 nt
	s_waitcnt vmcnt(28)
	v_add_f32_e32 v128, v128, v129
	v_add_f32_e32 v130, v130, v131
	v_add_f32_e32 v132, v132, v133
	v_add_f32_e32 v134, v134, v135
	v_add_f32_e32 v136, v136, v137
	v_add_f32_e32 v138, v138, v139
	v_add_f32_e32 v140, v140, v141
	v_add_f32_e32 v142, v142, v143
	v_add_f32_e32 v128, v128, v130
	v_add_f32_e32 v132, v132, v134
	v_add_f32_e32 v136, v136, v138
	v_add_f32_e32 v140, v140, v142
	v_cndmask_b32_e64 v130, v128, v132, s[30:31]
	v_cndmask_b32_e64 v134, v136, v140, s[30:31]
	v_cndmask_b32_e64 v129, v132, v128, s[30:31]
	v_cndmask_b32_e64 v133, v140, v136, s[30:31]
	v_add_f32_dpp v129, v130, v129 quad_perm:[1,0,3,2] row_mask:0xf bank_mask:0xf bound_ctrl:1
	v_add_f32_dpp v133, v134, v133 quad_perm:[1,0,3,2] row_mask:0xf bank_mask:0xf bound_ctrl:1
	v_cndmask_b32_e64 v135, v129, v133, s[32:33]
	v_cndmask_b32_e64 v131, v133, v129, s[32:33]
	s_nop 1
	v_add_f32_dpp v131, v135, v131 quad_perm:[2,3,0,1] row_mask:0xf bank_mask:0xf bound_ctrl:1
	v_cvt_f16_f32_e32 v131, v131
	ds_write_b16 v14, v131 offset:0
	s_waitcnt vmcnt(24)
	v_add_f32_e32 v144, v144, v145
	v_add_f32_e32 v146, v146, v147
	v_add_f32_e32 v148, v148, v149
	v_add_f32_e32 v150, v150, v151
	v_add_f32_e32 v152, v152, v153
	v_add_f32_e32 v154, v154, v155
	v_add_f32_e32 v156, v156, v157
	v_add_f32_e32 v158, v158, v159
	v_add_f32_e32 v144, v144, v146
	v_add_f32_e32 v148, v148, v150
	v_add_f32_e32 v152, v152, v154
	v_add_f32_e32 v156, v156, v158
	v_cndmask_b32_e64 v146, v144, v148, s[30:31]
	v_cndmask_b32_e64 v150, v152, v156, s[30:31]
	v_cndmask_b32_e64 v145, v148, v144, s[30:31]
	v_cndmask_b32_e64 v149, v156, v152, s[30:31]
	v_add_f32_dpp v145, v146, v145 quad_perm:[1,0,3,2] row_mask:0xf bank_mask:0xf bound_ctrl:1
	v_add_f32_dpp v149, v150, v149 quad_perm:[1,0,3,2] row_mask:0xf bank_mask:0xf bound_ctrl:1
	v_cndmask_b32_e64 v151, v145, v149, s[32:33]
	v_cndmask_b32_e64 v147, v149, v145, s[32:33]
	s_nop 1
	v_add_f32_dpp v147, v151, v147 quad_perm:[2,3,0,1] row_mask:0xf bank_mask:0xf bound_ctrl:1
	v_cvt_f16_f32_e32 v147, v147
	ds_write_b16 v14, v147 offset:1088
	s_waitcnt vmcnt(20)
	v_add_f32_e32 v160, v160, v161
	v_add_f32_e32 v162, v162, v163
	v_add_f32_e32 v164, v164, v165
	v_add_f32_e32 v166, v166, v167
	v_add_f32_e32 v168, v168, v169
	v_add_f32_e32 v170, v170, v171
	v_add_f32_e32 v172, v172, v173
	v_add_f32_e32 v174, v174, v175
	v_add_f32_e32 v160, v160, v162
	v_add_f32_e32 v164, v164, v166
	v_add_f32_e32 v168, v168, v170
	v_add_f32_e32 v172, v172, v174
	v_cndmask_b32_e64 v162, v160, v164, s[30:31]
	v_cndmask_b32_e64 v166, v168, v172, s[30:31]
	v_cndmask_b32_e64 v161, v164, v160, s[30:31]
	v_cndmask_b32_e64 v165, v172, v168, s[30:31]
	v_add_f32_dpp v161, v162, v161 quad_perm:[1,0,3,2] row_mask:0xf bank_mask:0xf bound_ctrl:1
	v_add_f32_dpp v165, v166, v165 quad_perm:[1,0,3,2] row_mask:0xf bank_mask:0xf bound_ctrl:1
	v_cndmask_b32_e64 v167, v161, v165, s[32:33]
	v_cndmask_b32_e64 v163, v165, v161, s[32:33]
	s_nop 1
	v_add_f32_dpp v163, v167, v163 quad_perm:[2,3,0,1] row_mask:0xf bank_mask:0xf bound_ctrl:1
	v_cvt_f16_f32_e32 v163, v163
	ds_write_b16 v14, v163 offset:2176
	s_waitcnt vmcnt(16)
	v_add_f32_e32 v176, v176, v177
	v_add_f32_e32 v178, v178, v179
	v_add_f32_e32 v180, v180, v181
	v_add_f32_e32 v182, v182, v183
	v_add_f32_e32 v184, v184, v185
	v_add_f32_e32 v186, v186, v187
	v_add_f32_e32 v188, v188, v189
	v_add_f32_e32 v190, v190, v191
	v_add_f32_e32 v176, v176, v178
	v_add_f32_e32 v180, v180, v182
	v_add_f32_e32 v184, v184, v186
	v_add_f32_e32 v188, v188, v190
	v_cndmask_b32_e64 v178, v176, v180, s[30:31]
	v_cndmask_b32_e64 v182, v184, v188, s[30:31]
	v_cndmask_b32_e64 v177, v180, v176, s[30:31]
	v_cndmask_b32_e64 v181, v188, v184, s[30:31]
	v_add_f32_dpp v177, v178, v177 quad_perm:[1,0,3,2] row_mask:0xf bank_mask:0xf bound_ctrl:1
	v_add_f32_dpp v181, v182, v181 quad_perm:[1,0,3,2] row_mask:0xf bank_mask:0xf bound_ctrl:1
	v_cndmask_b32_e64 v183, v177, v181, s[32:33]
	v_cndmask_b32_e64 v179, v181, v177, s[32:33]
	s_nop 1
	v_add_f32_dpp v179, v183, v179 quad_perm:[2,3,0,1] row_mask:0xf bank_mask:0xf bound_ctrl:1
	v_cvt_f16_f32_e32 v179, v179
	ds_write_b16 v14, v179 offset:3264
	s_mov_b32 s29, 0
	v_mov_b32_e32 v160, 0
	v_mov_b32_e32 v161, 0
	v_mov_b32_e32 v162, 0
	v_mov_b32_e32 v163, 0
	s_lshl_b32 s6, s6, 6
	s_add_i32 s6, s6, s7
	s_lshl_b32 s6, s6, 10
	v_add_u32_e32 v5, s6, v5
	s_branch .Lpass
